# v10 + leading wave group of the MoE GEMM loops waits for its LDS-DMA loads after its MFMA block (before the second barrier) instead of before the first
# baseline (speedup 1.0000x reference)
.LBB0_832:
	s_add_u32 s44, s40, 0xed800100
	v_add_u32_e32 v1, s62, v158
	s_addc_u32 s45, s41, -1
	ds_read_b128 v[146:149], v1
	ds_read_b128 v[150:153], v1 offset:1024
	ds_read_b128 v[160:163], v1 offset:2048
	ds_read_b128 v[164:167], v1 offset:3072
	v_add_u32_e32 v1, s63, v158
	s_add_u32 s46, s18, s40
	ds_read_b128 v[168:171], v1
	ds_read_b128 v[172:175], v1 offset:1024
	ds_read_b128 v[176:179], v1 offset:2048
	ds_read_b128 v[180:183], v1 offset:3072
	s_addc_u32 s47, s19, s41
	s_add_u32 s46, s46, 0xed800100
	s_addc_u32 s47, s47, -1
	s_and_b64 s[42:43], s[42:43], exec
	s_cselect_b32 s42, s0, s46
	s_cselect_b32 s43, s1, s47
	s_cselect_b32 s69, s39, s45
	s_cselect_b32 s70, s38, s44
	s_add_u32 s44, s42, 0x80
	s_addc_u32 s45, s43, 0
	s_add_u32 s46, s90, s40
	s_addc_u32 s47, s91, s41
	s_add_u32 s46, s46, 0x80
	s_addc_u32 s47, s47, 0
	s_add_i32 m0, s7, 0xc000
	ds_read_b128 v[184:187], v143
	ds_read_b128 v[188:191], v143 offset:1024
	ds_read_b128 v[192:195], v143 offset:2048
	ds_read_b128 v[196:199], v143 offset:3072
	ds_read_b128 v[200:203], v143 offset:4096
	ds_read_b128 v[204:207], v143 offset:5120
	ds_read_b128 v[208:211], v143 offset:6144
	ds_read_b128 v[212:215], v143 offset:7168
	s_nop 0
	global_load_lds_dwordx4 v2, s[46:47]
	s_add_i32 m0, s7, 0xe000
	s_nop 0
	global_load_lds_dwordx4 v3, s[46:47]
	s_cmp_lg_u64 s[20:21], 0
	s_cbranch_scc0 .Lgw_p6a_0
	s_waitcnt vmcnt(8)
.Lgw_p6a_0:
	s_waitcnt lgkmcnt(0)
	s_barrier
	s_setprio 1
	s_waitcnt lgkmcnt(0)
	v_mfma_scale_f32_16x16x128_f8f6f4 v[128:131], v[146:153], v[184:191], v[128:131], v145, v145 op_sel_hi:[0,0,0]
	v_mfma_scale_f32_16x16x128_f8f6f4 v[124:127], v[160:167], v[184:191], v[124:127], v145, v145 op_sel_hi:[0,0,0]
	v_mfma_scale_f32_16x16x128_f8f6f4 v[120:123], v[146:153], v[192:199], v[120:123], v145, v145 op_sel_hi:[0,0,0]
	v_mfma_scale_f32_16x16x128_f8f6f4 v[116:119], v[160:167], v[192:199], v[116:119], v145, v145 op_sel_hi:[0,0,0]
	v_mfma_scale_f32_16x16x128_f8f6f4 v[112:115], v[146:153], v[200:207], v[112:115], v145, v145 op_sel_hi:[0,0,0]
	v_mfma_scale_f32_16x16x128_f8f6f4 v[108:111], v[160:167], v[200:207], v[108:111], v145, v145 op_sel_hi:[0,0,0]
	v_mfma_scale_f32_16x16x128_f8f6f4 v[104:107], v[146:153], v[208:215], v[104:107], v145, v145 op_sel_hi:[0,0,0]
	v_mfma_scale_f32_16x16x128_f8f6f4 v[100:103], v[160:167], v[208:215], v[100:103], v145, v145 op_sel_hi:[0,0,0]
	s_setprio 0
	s_setprio 1
	v_mfma_scale_f32_16x16x128_f8f6f4 v[136:139], v[168:175], v[184:191], v[96:99], v145, v145 op_sel_hi:[0,0,0]
	v_mfma_scale_f32_16x16x128_f8f6f4 v[184:187], v[176:183], v[184:191], v[92:95], v145, v145 op_sel_hi:[0,0,0]
	v_mfma_scale_f32_16x16x128_f8f6f4 v[188:191], v[168:175], v[192:199], v[88:91], v145, v145 op_sel_hi:[0,0,0]
	v_mfma_scale_f32_16x16x128_f8f6f4 v[192:195], v[176:183], v[192:199], v[84:87], v145, v145 op_sel_hi:[0,0,0]
	v_mfma_scale_f32_16x16x128_f8f6f4 v[196:199], v[168:175], v[200:207], v[80:83], v145, v145 op_sel_hi:[0,0,0]
	v_mfma_scale_f32_16x16x128_f8f6f4 v[200:203], v[176:183], v[200:207], v[76:79], v145, v145 op_sel_hi:[0,0,0]
	v_mfma_scale_f32_16x16x128_f8f6f4 v[204:207], v[168:175], v[208:215], v[72:75], v145, v145 op_sel_hi:[0,0,0]
	v_mfma_scale_f32_16x16x128_f8f6f4 v[208:211], v[176:183], v[208:215], v[28:31], v145, v145 op_sel_hi:[0,0,0]
	s_setprio 0
	s_waitcnt vmcnt(8)
	s_barrier
	s_add_i32 s71, s62, s52
	s_mov_b64 s[46:47], s[42:43]
	s_mov_b32 m0, s71
	ds_read_b128 v[68:71], v143 offset:16384
	ds_read_b128 v[72:75], v143 offset:17408
	ds_read_b128 v[76:79], v143 offset:18432
	ds_read_b128 v[80:83], v143 offset:19456
	ds_read_b128 v[84:87], v143 offset:20480
	ds_read_b128 v[88:91], v143 offset:21504
	ds_read_b128 v[92:95], v143 offset:22528
	ds_read_b128 v[96:99], v143 offset:23552
	s_nop 0
	global_load_lds_dwordx4 v140, s[46:47]
	s_add_i32 m0, s71, 0x2000
	s_nop 0
	global_load_lds_dwordx4 v142, s[46:47]
	s_add_u32 s46, s42, 0x40000
	s_addc_u32 s47, s43, 0
	s_add_i32 s71, s63, s52
	s_mov_b32 m0, s71
	s_nop 0
	global_load_lds_dwordx4 v140, s[46:47]
	s_add_i32 m0, s71, 0x2000
	s_nop 0
	global_load_lds_dwordx4 v142, s[46:47]
	s_add_u32 s46, s16, s70
	s_addc_u32 s47, s17, s69
	s_mov_b64 s[70:71], s[46:47]
	s_mov_b32 m0, s7
	s_nop 0
	global_load_lds_dwordx4 v132, s[70:71]
	s_mov_b32 m0, s25
	s_nop 0
	global_load_lds_dwordx4 v133, s[70:71]
	s_cmp_lg_u64 s[20:21], 0
	s_cbranch_scc0 .Lgw_p6a_1
	s_waitcnt vmcnt(8)
.Lgw_p6a_1:
	s_waitcnt lgkmcnt(0)
	s_barrier
	s_setprio 1
	s_waitcnt lgkmcnt(0)
	v_mfma_scale_f32_16x16x128_f8f6f4 v[64:67], v[146:153], v[68:75], v[64:67], v145, v145 op_sel_hi:[0,0,0]
	v_mfma_scale_f32_16x16x128_f8f6f4 v[60:63], v[160:167], v[68:75], v[60:63], v145, v145 op_sel_hi:[0,0,0]
	v_mfma_scale_f32_16x16x128_f8f6f4 v[56:59], v[146:153], v[76:83], v[56:59], v145, v145 op_sel_hi:[0,0,0]
	v_mfma_scale_f32_16x16x128_f8f6f4 v[52:55], v[160:167], v[76:83], v[52:55], v145, v145 op_sel_hi:[0,0,0]
	v_mfma_scale_f32_16x16x128_f8f6f4 v[212:215], v[146:153], v[84:91], v[48:51], v145, v145 op_sel_hi:[0,0,0]
	v_mfma_scale_f32_16x16x128_f8f6f4 v[216:219], v[160:167], v[84:91], v[44:47], v145, v145 op_sel_hi:[0,0,0]
	v_mfma_scale_f32_16x16x128_f8f6f4 v[220:223], v[146:153], v[92:99], v[40:43], v145, v145 op_sel_hi:[0,0,0]
	v_mfma_scale_f32_16x16x128_f8f6f4 v[224:227], v[160:167], v[92:99], v[36:39], v145, v145 op_sel_hi:[0,0,0]
	s_setprio 0
	s_setprio 1
	v_mfma_scale_f32_16x16x128_f8f6f4 v[232:235], v[176:183], v[68:75], v[232:235], v145, v145 op_sel_hi:[0,0,0]
	v_mfma_scale_f32_16x16x128_f8f6f4 v[228:231], v[168:175], v[68:75], v[32:35], v145, v145 op_sel_hi:[0,0,0]
	v_mfma_scale_f32_16x16x128_f8f6f4 v[236:239], v[168:175], v[76:83], v[24:27], v145, v145 op_sel_hi:[0,0,0]
	v_mfma_scale_f32_16x16x128_f8f6f4 v[240:243], v[176:183], v[76:83], v[20:23], v145, v145 op_sel_hi:[0,0,0]
	v_mfma_scale_f32_16x16x128_f8f6f4 v[244:247], v[168:175], v[84:91], v[16:19], v145, v145 op_sel_hi:[0,0,0]
	v_mfma_scale_f32_16x16x128_f8f6f4 v[248:251], v[176:183], v[84:91], v[12:15], v145, v145 op_sel_hi:[0,0,0]
	v_mfma_scale_f32_16x16x128_f8f6f4 v[154:157], v[168:175], v[92:99], v[8:11], v145, v145 op_sel_hi:[0,0,0]
	v_mfma_scale_f32_16x16x128_f8f6f4 v[68:71], v[176:183], v[92:99], v[4:7], v145, v145 op_sel_hi:[0,0,0]
	s_setprio 0
	s_waitcnt vmcnt(8)
	s_barrier
	s_add_i32 s69, 0, 0x18000
	v_add_u32_e32 v1, s69, v158
	s_add_i32 s72, 0, 0x1c000
	s_nop 1
	ds_read_b128 v[4:7], v1
	ds_read_b128 v[8:11], v1 offset:1024
	ds_read_b128 v[12:15], v1 offset:2048
	ds_read_b128 v[16:19], v1 offset:3072
	v_add_u32_e32 v1, s72, v158
	ds_read_b128 v[146:149], v1
	ds_read_b128 v[150:153], v1 offset:1024
	ds_read_b128 v[160:163], v1 offset:2048
	ds_read_b128 v[164:167], v1 offset:3072
	s_mov_b64 s[70:71], s[46:47]
	s_mov_b32 m0, s33
	ds_read_b128 v[20:23], v143 offset:32768
	ds_read_b128 v[24:27], v143 offset:33792
	ds_read_b128 v[28:31], v143 offset:34816
	ds_read_b128 v[32:35], v143 offset:35840
	ds_read_b128 v[36:39], v143 offset:36864
	ds_read_b128 v[40:43], v143 offset:37888
	ds_read_b128 v[44:47], v143 offset:38912
	ds_read_b128 v[48:51], v143 offset:39936
	s_nop 0
	global_load_lds_dwordx4 v134, s[70:71]
	s_mov_b32 m0, s58
	s_nop 0
	global_load_lds_dwordx4 v135, s[70:71]
	s_cmp_lg_u64 s[20:21], 0
	s_cbranch_scc0 .Lgw_p6a_2
	s_waitcnt vmcnt(8)
.Lgw_p6a_2:
	s_waitcnt lgkmcnt(0)
	s_barrier
	s_setprio 1
	s_waitcnt lgkmcnt(0)
	v_mfma_scale_f32_16x16x128_f8f6f4 v[128:131], v[4:11], v[20:27], v[128:131], v145, v145 op_sel_hi:[0,0,0]
	v_mfma_scale_f32_16x16x128_f8f6f4 v[124:127], v[12:19], v[20:27], v[124:127], v145, v145 op_sel_hi:[0,0,0]
	v_mfma_scale_f32_16x16x128_f8f6f4 v[120:123], v[4:11], v[28:35], v[120:123], v145, v145 op_sel_hi:[0,0,0]
	v_mfma_scale_f32_16x16x128_f8f6f4 v[116:119], v[12:19], v[28:35], v[116:119], v145, v145 op_sel_hi:[0,0,0]
	v_mfma_scale_f32_16x16x128_f8f6f4 v[112:115], v[4:11], v[36:43], v[112:115], v145, v145 op_sel_hi:[0,0,0]
	v_mfma_scale_f32_16x16x128_f8f6f4 v[108:111], v[12:19], v[36:43], v[108:111], v145, v145 op_sel_hi:[0,0,0]
	v_mfma_scale_f32_16x16x128_f8f6f4 v[104:107], v[4:11], v[44:51], v[104:107], v145, v145 op_sel_hi:[0,0,0]
	v_mfma_scale_f32_16x16x128_f8f6f4 v[100:103], v[12:19], v[44:51], v[100:103], v145, v145 op_sel_hi:[0,0,0]
	s_setprio 0
	s_setprio 1
	v_mfma_scale_f32_16x16x128_f8f6f4 v[96:99], v[146:153], v[20:27], v[136:139], v145, v145 op_sel_hi:[0,0,0]
	v_mfma_scale_f32_16x16x128_f8f6f4 v[92:95], v[160:167], v[20:27], v[184:187], v145, v145 op_sel_hi:[0,0,0]
	v_mfma_scale_f32_16x16x128_f8f6f4 v[88:91], v[146:153], v[28:35], v[188:191], v145, v145 op_sel_hi:[0,0,0]
	v_mfma_scale_f32_16x16x128_f8f6f4 v[84:87], v[160:167], v[28:35], v[192:195], v145, v145 op_sel_hi:[0,0,0]
	v_mfma_scale_f32_16x16x128_f8f6f4 v[80:83], v[146:153], v[36:43], v[196:199], v145, v145 op_sel_hi:[0,0,0]
	v_mfma_scale_f32_16x16x128_f8f6f4 v[76:79], v[160:167], v[36:43], v[200:203], v145, v145 op_sel_hi:[0,0,0]
	v_mfma_scale_f32_16x16x128_f8f6f4 v[72:75], v[146:153], v[44:51], v[204:207], v145, v145 op_sel_hi:[0,0,0]
	v_mfma_scale_f32_16x16x128_f8f6f4 v[28:31], v[160:167], v[44:51], v[208:211], v145, v145 op_sel_hi:[0,0,0]
	s_setprio 0
	s_waitcnt vmcnt(8)
	s_barrier
	s_add_i32 s69, s69, s52
	s_mov_b32 m0, s69
	ds_read_b128 v[20:23], v143 offset:49152
	ds_read_b128 v[24:27], v143 offset:50176
	ds_read_b128 v[168:171], v143 offset:51200
	ds_read_b128 v[172:175], v143 offset:52224
	ds_read_b128 v[176:179], v143 offset:53248
	ds_read_b128 v[180:183], v143 offset:54272
	ds_read_b128 v[184:187], v143 offset:55296
	ds_read_b128 v[188:191], v143 offset:56320
	s_nop 0
	global_load_lds_dwordx4 v140, s[44:45]
	s_add_i32 m0, s69, 0x2000
	s_add_u32 s42, s42, 0x40080
	global_load_lds_dwordx4 v142, s[44:45]
	s_addc_u32 s43, s43, 0
	s_add_i32 s44, s72, s52
	s_mov_b32 m0, s44
	s_nop 0
	global_load_lds_dwordx4 v140, s[42:43]
	s_add_i32 m0, s44, 0x2000
	s_nop 0
	global_load_lds_dwordx4 v142, s[42:43]
	s_add_u32 s42, s46, 0x80
	s_addc_u32 s43, s47, 0
	s_mov_b32 m0, s60
	s_nop 0
	global_load_lds_dwordx4 v132, s[42:43]
	s_mov_b32 m0, s61
	s_nop 0
	global_load_lds_dwordx4 v133, s[42:43]
	s_cmp_lg_u64 s[20:21], 0
	s_cbranch_scc0 .Lgw_p6a_3
	s_waitcnt vmcnt(8)
.Lgw_p6a_3:
	s_waitcnt lgkmcnt(0)
	s_barrier
	s_setprio 1
	s_waitcnt lgkmcnt(0)
	v_mfma_scale_f32_16x16x128_f8f6f4 v[64:67], v[4:11], v[20:27], v[64:67], v145, v145 op_sel_hi:[0,0,0]
	v_mfma_scale_f32_16x16x128_f8f6f4 v[60:63], v[12:19], v[20:27], v[60:63], v145, v145 op_sel_hi:[0,0,0]
	v_mfma_scale_f32_16x16x128_f8f6f4 v[56:59], v[4:11], v[168:175], v[56:59], v145, v145 op_sel_hi:[0,0,0]
	v_mfma_scale_f32_16x16x128_f8f6f4 v[52:55], v[12:19], v[168:175], v[52:55], v145, v145 op_sel_hi:[0,0,0]
	v_mfma_scale_f32_16x16x128_f8f6f4 v[48:51], v[4:11], v[176:183], v[212:215], v145, v145 op_sel_hi:[0,0,0]
	v_mfma_scale_f32_16x16x128_f8f6f4 v[44:47], v[12:19], v[176:183], v[216:219], v145, v145 op_sel_hi:[0,0,0]
	v_mfma_scale_f32_16x16x128_f8f6f4 v[40:43], v[4:11], v[184:191], v[220:223], v145, v145 op_sel_hi:[0,0,0]
	v_mfma_scale_f32_16x16x128_f8f6f4 v[36:39], v[12:19], v[184:191], v[224:227], v145, v145 op_sel_hi:[0,0,0]
	s_setprio 0
	s_setprio 1
	v_mfma_scale_f32_16x16x128_f8f6f4 v[32:35], v[146:153], v[20:27], v[228:231], v145, v145 op_sel_hi:[0,0,0]
	v_mfma_scale_f32_16x16x128_f8f6f4 v[232:235], v[160:167], v[20:27], v[232:235], v145, v145 op_sel_hi:[0,0,0]
	v_mfma_scale_f32_16x16x128_f8f6f4 v[24:27], v[146:153], v[168:175], v[236:239], v145, v145 op_sel_hi:[0,0,0]
	v_mfma_scale_f32_16x16x128_f8f6f4 v[20:23], v[160:167], v[168:175], v[240:243], v145, v145 op_sel_hi:[0,0,0]
	v_mfma_scale_f32_16x16x128_f8f6f4 v[16:19], v[146:153], v[176:183], v[244:247], v145, v145 op_sel_hi:[0,0,0]
	v_mfma_scale_f32_16x16x128_f8f6f4 v[12:15], v[160:167], v[176:183], v[248:251], v145, v145 op_sel_hi:[0,0,0]
	v_mfma_scale_f32_16x16x128_f8f6f4 v[8:11], v[146:153], v[184:191], v[154:157], v145, v145 op_sel_hi:[0,0,0]
	v_mfma_scale_f32_16x16x128_f8f6f4 v[4:7], v[160:167], v[184:191], v[68:71], v145, v145 op_sel_hi:[0,0,0]
	s_setprio 0
	s_waitcnt vmcnt(8)
	s_barrier
	s_add_i32 s5, s5, 2
	s_add_u32 s40, s40, 0x100
	s_addc_u32 s41, s41, 0
	s_cmp_gt_u32 s5, 13
	s_cbranch_scc1 .LBB0_835

.LBB0_917:
	s_add_u32 s44, s40, 0xed800100
	v_add_u32_e32 v1, s57, v158
	s_addc_u32 s45, s41, -1
	ds_read_b128 v[146:149], v1
	ds_read_b128 v[150:153], v1 offset:1024
	ds_read_b128 v[160:163], v1 offset:2048
	ds_read_b128 v[164:167], v1 offset:3072
	v_add_u32_e32 v1, s61, v158
	s_add_u32 s46, s18, s40
	ds_read_b128 v[168:171], v1
	ds_read_b128 v[172:175], v1 offset:1024
	ds_read_b128 v[176:179], v1 offset:2048
	ds_read_b128 v[180:183], v1 offset:3072
	s_addc_u32 s47, s19, s41
	s_add_u32 s46, s46, 0xed800100
	s_addc_u32 s47, s47, -1
	s_and_b64 s[42:43], s[42:43], exec
	s_cselect_b32 s42, s0, s46
	s_cselect_b32 s43, s1, s47
	s_cselect_b32 s68, s39, s45
	s_cselect_b32 s69, s38, s44
	s_add_u32 s44, s42, 0x80
	s_addc_u32 s45, s43, 0
	s_add_u32 s46, s90, s40
	s_addc_u32 s47, s91, s41
	s_add_u32 s46, s46, 0x80
	s_addc_u32 s47, s47, 0
	s_add_i32 m0, s7, 0xc000
	ds_read_b128 v[184:187], v143
	ds_read_b128 v[188:191], v143 offset:1024
	ds_read_b128 v[192:195], v143 offset:2048
	ds_read_b128 v[196:199], v143 offset:3072
	ds_read_b128 v[200:203], v143 offset:4096
	ds_read_b128 v[204:207], v143 offset:5120
	ds_read_b128 v[208:211], v143 offset:6144
	ds_read_b128 v[212:215], v143 offset:7168
	s_nop 0
	global_load_lds_dwordx4 v2, s[46:47]
	s_add_i32 m0, s7, 0xe000
	s_nop 0
	global_load_lds_dwordx4 v3, s[46:47]
	s_cmp_lg_u64 s[20:21], 0
	s_cbranch_scc0 .Lgw_p6b_0
	s_waitcnt vmcnt(8)
.Lgw_p6b_0:
	s_waitcnt lgkmcnt(0)
	s_barrier
	s_setprio 1
	s_waitcnt lgkmcnt(0)
	v_mfma_scale_f32_16x16x128_f8f6f4 v[128:131], v[146:153], v[184:191], v[128:131], v145, v145 op_sel_hi:[0,0,0]
	v_mfma_scale_f32_16x16x128_f8f6f4 v[124:127], v[160:167], v[184:191], v[124:127], v145, v145 op_sel_hi:[0,0,0]
	v_mfma_scale_f32_16x16x128_f8f6f4 v[120:123], v[146:153], v[192:199], v[120:123], v145, v145 op_sel_hi:[0,0,0]
	v_mfma_scale_f32_16x16x128_f8f6f4 v[116:119], v[160:167], v[192:199], v[116:119], v145, v145 op_sel_hi:[0,0,0]
	v_mfma_scale_f32_16x16x128_f8f6f4 v[112:115], v[146:153], v[200:207], v[112:115], v145, v145 op_sel_hi:[0,0,0]
	v_mfma_scale_f32_16x16x128_f8f6f4 v[108:111], v[160:167], v[200:207], v[108:111], v145, v145 op_sel_hi:[0,0,0]
	v_mfma_scale_f32_16x16x128_f8f6f4 v[104:107], v[146:153], v[208:215], v[104:107], v145, v145 op_sel_hi:[0,0,0]
	v_mfma_scale_f32_16x16x128_f8f6f4 v[100:103], v[160:167], v[208:215], v[100:103], v145, v145 op_sel_hi:[0,0,0]
	s_setprio 0
	s_setprio 1
	v_mfma_scale_f32_16x16x128_f8f6f4 v[136:139], v[168:175], v[184:191], v[96:99], v145, v145 op_sel_hi:[0,0,0]
	v_mfma_scale_f32_16x16x128_f8f6f4 v[184:187], v[176:183], v[184:191], v[92:95], v145, v145 op_sel_hi:[0,0,0]
	v_mfma_scale_f32_16x16x128_f8f6f4 v[188:191], v[168:175], v[192:199], v[88:91], v145, v145 op_sel_hi:[0,0,0]
	v_mfma_scale_f32_16x16x128_f8f6f4 v[192:195], v[176:183], v[192:199], v[84:87], v145, v145 op_sel_hi:[0,0,0]
	v_mfma_scale_f32_16x16x128_f8f6f4 v[196:199], v[168:175], v[200:207], v[80:83], v145, v145 op_sel_hi:[0,0,0]
	v_mfma_scale_f32_16x16x128_f8f6f4 v[200:203], v[176:183], v[200:207], v[76:79], v145, v145 op_sel_hi:[0,0,0]
	v_mfma_scale_f32_16x16x128_f8f6f4 v[204:207], v[168:175], v[208:215], v[72:75], v145, v145 op_sel_hi:[0,0,0]
	v_mfma_scale_f32_16x16x128_f8f6f4 v[208:211], v[176:183], v[208:215], v[28:31], v145, v145 op_sel_hi:[0,0,0]
	s_setprio 0
	s_waitcnt vmcnt(8)
	s_barrier
	s_add_i32 s70, s57, s52
	s_mov_b64 s[46:47], s[42:43]
	s_mov_b32 m0, s70
	ds_read_b128 v[68:71], v143 offset:16384
	ds_read_b128 v[72:75], v143 offset:17408
	ds_read_b128 v[76:79], v143 offset:18432
	ds_read_b128 v[80:83], v143 offset:19456
	ds_read_b128 v[84:87], v143 offset:20480
	ds_read_b128 v[88:91], v143 offset:21504
	ds_read_b128 v[92:95], v143 offset:22528
	ds_read_b128 v[96:99], v143 offset:23552
	s_nop 0
	global_load_lds_dwordx4 v140, s[46:47]
	s_add_i32 m0, s70, 0x2000
	s_nop 0
	global_load_lds_dwordx4 v142, s[46:47]
	s_add_u32 s46, s42, 0x40000
	s_addc_u32 s47, s43, 0
	s_add_i32 s70, s61, s52
	s_mov_b32 m0, s70
	s_nop 0
	global_load_lds_dwordx4 v140, s[46:47]
	s_add_i32 m0, s70, 0x2000
	s_nop 0
	global_load_lds_dwordx4 v142, s[46:47]
	s_add_u32 s46, s16, s69
	s_addc_u32 s47, s17, s68
	s_mov_b64 s[68:69], s[46:47]
	s_mov_b32 m0, s7
	s_nop 0
	global_load_lds_dwordx4 v132, s[68:69]
	s_mov_b32 m0, s25
	s_nop 0
	global_load_lds_dwordx4 v133, s[68:69]
	s_cmp_lg_u64 s[20:21], 0
	s_cbranch_scc0 .Lgw_p6b_1
	s_waitcnt vmcnt(8)
.Lgw_p6b_1:
	s_waitcnt lgkmcnt(0)
	s_barrier
	s_setprio 1
	s_waitcnt lgkmcnt(0)
	v_mfma_scale_f32_16x16x128_f8f6f4 v[64:67], v[146:153], v[68:75], v[64:67], v145, v145 op_sel_hi:[0,0,0]
	v_mfma_scale_f32_16x16x128_f8f6f4 v[60:63], v[160:167], v[68:75], v[60:63], v145, v145 op_sel_hi:[0,0,0]
	v_mfma_scale_f32_16x16x128_f8f6f4 v[56:59], v[146:153], v[76:83], v[56:59], v145, v145 op_sel_hi:[0,0,0]
	v_mfma_scale_f32_16x16x128_f8f6f4 v[52:55], v[160:167], v[76:83], v[52:55], v145, v145 op_sel_hi:[0,0,0]
	v_mfma_scale_f32_16x16x128_f8f6f4 v[212:215], v[146:153], v[84:91], v[48:51], v145, v145 op_sel_hi:[0,0,0]
	v_mfma_scale_f32_16x16x128_f8f6f4 v[216:219], v[160:167], v[84:91], v[44:47], v145, v145 op_sel_hi:[0,0,0]
	v_mfma_scale_f32_16x16x128_f8f6f4 v[220:223], v[146:153], v[92:99], v[40:43], v145, v145 op_sel_hi:[0,0,0]
	v_mfma_scale_f32_16x16x128_f8f6f4 v[224:227], v[160:167], v[92:99], v[36:39], v145, v145 op_sel_hi:[0,0,0]
	s_setprio 0
	s_setprio 1
	v_mfma_scale_f32_16x16x128_f8f6f4 v[232:235], v[176:183], v[68:75], v[232:235], v145, v145 op_sel_hi:[0,0,0]
	v_mfma_scale_f32_16x16x128_f8f6f4 v[228:231], v[168:175], v[68:75], v[32:35], v145, v145 op_sel_hi:[0,0,0]
	v_mfma_scale_f32_16x16x128_f8f6f4 v[236:239], v[168:175], v[76:83], v[24:27], v145, v145 op_sel_hi:[0,0,0]
	v_mfma_scale_f32_16x16x128_f8f6f4 v[240:243], v[176:183], v[76:83], v[20:23], v145, v145 op_sel_hi:[0,0,0]
	v_mfma_scale_f32_16x16x128_f8f6f4 v[244:247], v[168:175], v[84:91], v[16:19], v145, v145 op_sel_hi:[0,0,0]
	v_mfma_scale_f32_16x16x128_f8f6f4 v[248:251], v[176:183], v[84:91], v[12:15], v145, v145 op_sel_hi:[0,0,0]
	v_mfma_scale_f32_16x16x128_f8f6f4 v[154:157], v[168:175], v[92:99], v[8:11], v145, v145 op_sel_hi:[0,0,0]
	v_mfma_scale_f32_16x16x128_f8f6f4 v[68:71], v[176:183], v[92:99], v[4:7], v145, v145 op_sel_hi:[0,0,0]
	s_setprio 0
	s_waitcnt vmcnt(8)
	s_barrier
	s_add_i32 s70, 0, 0x18000
	v_add_u32_e32 v1, s70, v158
	s_add_i32 s71, 0, 0x1c000
	s_nop 1
	ds_read_b128 v[4:7], v1
	ds_read_b128 v[8:11], v1 offset:1024
	ds_read_b128 v[12:15], v1 offset:2048
	ds_read_b128 v[16:19], v1 offset:3072
	v_add_u32_e32 v1, s71, v158
	ds_read_b128 v[146:149], v1
	ds_read_b128 v[150:153], v1 offset:1024
	ds_read_b128 v[160:163], v1 offset:2048
	ds_read_b128 v[164:167], v1 offset:3072
	s_mov_b64 s[68:69], s[46:47]
	s_mov_b32 m0, s33
	ds_read_b128 v[20:23], v143 offset:32768
	ds_read_b128 v[24:27], v143 offset:33792
	ds_read_b128 v[28:31], v143 offset:34816
	ds_read_b128 v[32:35], v143 offset:35840
	ds_read_b128 v[36:39], v143 offset:36864
	ds_read_b128 v[40:43], v143 offset:37888
	ds_read_b128 v[44:47], v143 offset:38912
	ds_read_b128 v[48:51], v143 offset:39936
	s_nop 0
	global_load_lds_dwordx4 v134, s[68:69]
	s_mov_b32 m0, s58
	s_nop 0
	global_load_lds_dwordx4 v135, s[68:69]
	s_cmp_lg_u64 s[20:21], 0
	s_cbranch_scc0 .Lgw_p6b_2
	s_waitcnt vmcnt(8)
.Lgw_p6b_2:
	s_waitcnt lgkmcnt(0)
	s_barrier
	s_setprio 1
	s_waitcnt lgkmcnt(0)
	v_mfma_scale_f32_16x16x128_f8f6f4 v[128:131], v[4:11], v[20:27], v[128:131], v145, v145 op_sel_hi:[0,0,0]
	v_mfma_scale_f32_16x16x128_f8f6f4 v[124:127], v[12:19], v[20:27], v[124:127], v145, v145 op_sel_hi:[0,0,0]
	v_mfma_scale_f32_16x16x128_f8f6f4 v[120:123], v[4:11], v[28:35], v[120:123], v145, v145 op_sel_hi:[0,0,0]
	v_mfma_scale_f32_16x16x128_f8f6f4 v[116:119], v[12:19], v[28:35], v[116:119], v145, v145 op_sel_hi:[0,0,0]
	v_mfma_scale_f32_16x16x128_f8f6f4 v[112:115], v[4:11], v[36:43], v[112:115], v145, v145 op_sel_hi:[0,0,0]
	v_mfma_scale_f32_16x16x128_f8f6f4 v[108:111], v[12:19], v[36:43], v[108:111], v145, v145 op_sel_hi:[0,0,0]
	v_mfma_scale_f32_16x16x128_f8f6f4 v[104:107], v[4:11], v[44:51], v[104:107], v145, v145 op_sel_hi:[0,0,0]
	v_mfma_scale_f32_16x16x128_f8f6f4 v[100:103], v[12:19], v[44:51], v[100:103], v145, v145 op_sel_hi:[0,0,0]
	s_setprio 0
	s_setprio 1
	v_mfma_scale_f32_16x16x128_f8f6f4 v[96:99], v[146:153], v[20:27], v[136:139], v145, v145 op_sel_hi:[0,0,0]
	v_mfma_scale_f32_16x16x128_f8f6f4 v[92:95], v[160:167], v[20:27], v[184:187], v145, v145 op_sel_hi:[0,0,0]
	v_mfma_scale_f32_16x16x128_f8f6f4 v[88:91], v[146:153], v[28:35], v[188:191], v145, v145 op_sel_hi:[0,0,0]
	v_mfma_scale_f32_16x16x128_f8f6f4 v[84:87], v[160:167], v[28:35], v[192:195], v145, v145 op_sel_hi:[0,0,0]
	v_mfma_scale_f32_16x16x128_f8f6f4 v[80:83], v[146:153], v[36:43], v[196:199], v145, v145 op_sel_hi:[0,0,0]
	v_mfma_scale_f32_16x16x128_f8f6f4 v[76:79], v[160:167], v[36:43], v[200:203], v145, v145 op_sel_hi:[0,0,0]
	v_mfma_scale_f32_16x16x128_f8f6f4 v[72:75], v[146:153], v[44:51], v[204:207], v145, v145 op_sel_hi:[0,0,0]
	v_mfma_scale_f32_16x16x128_f8f6f4 v[28:31], v[160:167], v[44:51], v[208:211], v145, v145 op_sel_hi:[0,0,0]
	s_setprio 0
	s_waitcnt vmcnt(8)
	s_barrier
	s_add_i32 s68, s70, s52
	s_mov_b32 m0, s68
	ds_read_b128 v[20:23], v143 offset:49152
	ds_read_b128 v[24:27], v143 offset:50176
	ds_read_b128 v[168:171], v143 offset:51200
	ds_read_b128 v[172:175], v143 offset:52224
	ds_read_b128 v[176:179], v143 offset:53248
	ds_read_b128 v[180:183], v143 offset:54272
	ds_read_b128 v[184:187], v143 offset:55296
	ds_read_b128 v[188:191], v143 offset:56320
	s_nop 0
	global_load_lds_dwordx4 v140, s[44:45]
	s_add_i32 m0, s68, 0x2000
	s_add_u32 s42, s42, 0x40080
	global_load_lds_dwordx4 v142, s[44:45]
	s_addc_u32 s43, s43, 0
	s_add_i32 s44, s71, s52
	s_mov_b32 m0, s44
	s_nop 0
	global_load_lds_dwordx4 v140, s[42:43]
	s_add_i32 m0, s44, 0x2000
	s_nop 0
	global_load_lds_dwordx4 v142, s[42:43]
	s_add_u32 s42, s46, 0x80
	s_addc_u32 s43, s47, 0
	s_mov_b32 m0, s55
	s_nop 0
	global_load_lds_dwordx4 v132, s[42:43]
	s_mov_b32 m0, s56
	s_nop 0
	global_load_lds_dwordx4 v133, s[42:43]
	s_cmp_lg_u64 s[20:21], 0
	s_cbranch_scc0 .Lgw_p6b_3
	s_waitcnt vmcnt(8)

.LBB0_1045:
	s_add_u32 s25, s40, 0xeb800100
	v_add_u32_e32 v1, s58, v158
	s_addc_u32 s27, s41, -1
	ds_read_b128 v[136:139], v1
	ds_read_b128 v[140:143], v1 offset:1024
	ds_read_b128 v[160:163], v1 offset:2048
	ds_read_b128 v[164:167], v1 offset:3072
	v_add_u32_e32 v1, s59, v158
	s_add_u32 s44, s12, s40
	ds_read_b128 v[168:171], v1
	ds_read_b128 v[172:175], v1 offset:1024
	ds_read_b128 v[176:179], v1 offset:2048
	ds_read_b128 v[180:183], v1 offset:3072
	s_addc_u32 s45, s13, s41
	s_add_u32 s44, s44, 0xeb800100
	s_addc_u32 s45, s45, -1
	s_and_b64 s[42:43], s[42:43], exec
	s_cselect_b32 s42, s34, s44
	s_cselect_b32 s43, s35, s45
	s_cselect_b32 s27, s39, s27
	s_cselect_b32 s25, s38, s25
	s_add_u32 s44, s42, 0x80
	s_addc_u32 s45, s43, 0
	s_add_u32 s46, s90, s40
	s_addc_u32 s47, s91, s41
	s_add_u32 s46, s46, 0x80
	s_addc_u32 s47, s47, 0
	s_add_i32 m0, s1, 0xc000
	ds_read_b128 v[184:187], v151
	ds_read_b128 v[188:191], v151 offset:1024
	ds_read_b128 v[192:195], v151 offset:2048
	ds_read_b128 v[196:199], v151 offset:3072
	ds_read_b128 v[200:203], v151 offset:4096
	ds_read_b128 v[204:207], v151 offset:5120
	ds_read_b128 v[208:211], v151 offset:6144
	ds_read_b128 v[212:215], v151 offset:7168
	s_nop 0
	global_load_lds_dwordx4 v2, s[46:47]
	s_add_i32 m0, s1, 0xe000
	s_nop 0
	global_load_lds_dwordx4 v3, s[46:47]
	s_cmp_lg_u64 s[14:15], 0
	s_cbranch_scc0 .Lgw_p7_0
	s_waitcnt vmcnt(8)
.Lgw_p7_0:
	s_waitcnt lgkmcnt(0)
	s_barrier
	s_setprio 1
	s_waitcnt lgkmcnt(0)
	v_mfma_scale_f32_16x16x128_f8f6f4 v[128:131], v[136:143], v[184:191], v[128:131], v153, v153 op_sel_hi:[0,0,0]
	v_mfma_scale_f32_16x16x128_f8f6f4 v[124:127], v[160:167], v[184:191], v[124:127], v153, v153 op_sel_hi:[0,0,0]
	v_mfma_scale_f32_16x16x128_f8f6f4 v[120:123], v[136:143], v[192:199], v[120:123], v153, v153 op_sel_hi:[0,0,0]
	v_mfma_scale_f32_16x16x128_f8f6f4 v[116:119], v[160:167], v[192:199], v[116:119], v153, v153 op_sel_hi:[0,0,0]
	v_mfma_scale_f32_16x16x128_f8f6f4 v[112:115], v[136:143], v[200:207], v[112:115], v153, v153 op_sel_hi:[0,0,0]
	v_mfma_scale_f32_16x16x128_f8f6f4 v[108:111], v[160:167], v[200:207], v[108:111], v153, v153 op_sel_hi:[0,0,0]
	v_mfma_scale_f32_16x16x128_f8f6f4 v[104:107], v[136:143], v[208:215], v[104:107], v153, v153 op_sel_hi:[0,0,0]
	v_mfma_scale_f32_16x16x128_f8f6f4 v[100:103], v[160:167], v[208:215], v[100:103], v153, v153 op_sel_hi:[0,0,0]
	s_setprio 0
	s_setprio 1
	v_mfma_scale_f32_16x16x128_f8f6f4 v[144:147], v[168:175], v[184:191], v[96:99], v153, v153 op_sel_hi:[0,0,0]
	v_mfma_scale_f32_16x16x128_f8f6f4 v[184:187], v[176:183], v[184:191], v[92:95], v153, v153 op_sel_hi:[0,0,0]
	v_mfma_scale_f32_16x16x128_f8f6f4 v[188:191], v[168:175], v[192:199], v[88:91], v153, v153 op_sel_hi:[0,0,0]
	v_mfma_scale_f32_16x16x128_f8f6f4 v[192:195], v[176:183], v[192:199], v[84:87], v153, v153 op_sel_hi:[0,0,0]
	v_mfma_scale_f32_16x16x128_f8f6f4 v[196:199], v[168:175], v[200:207], v[80:83], v153, v153 op_sel_hi:[0,0,0]
	v_mfma_scale_f32_16x16x128_f8f6f4 v[200:203], v[176:183], v[200:207], v[76:79], v153, v153 op_sel_hi:[0,0,0]
	v_mfma_scale_f32_16x16x128_f8f6f4 v[204:207], v[168:175], v[208:215], v[72:75], v153, v153 op_sel_hi:[0,0,0]
	v_mfma_scale_f32_16x16x128_f8f6f4 v[208:211], v[176:183], v[208:215], v[28:31], v153, v153 op_sel_hi:[0,0,0]
	s_setprio 0
	s_waitcnt vmcnt(8)
	s_barrier
	s_add_i32 s64, s58, s48
	s_mov_b64 s[46:47], s[42:43]
	s_mov_b32 m0, s64
	ds_read_b128 v[68:71], v151 offset:16384
	ds_read_b128 v[72:75], v151 offset:17408
	ds_read_b128 v[76:79], v151 offset:18432
	ds_read_b128 v[80:83], v151 offset:19456
	ds_read_b128 v[84:87], v151 offset:20480
	ds_read_b128 v[88:91], v151 offset:21504
	ds_read_b128 v[92:95], v151 offset:22528
	ds_read_b128 v[96:99], v151 offset:23552
	s_nop 0
	global_load_lds_dwordx4 v148, s[46:47]
	s_add_i32 m0, s64, 0x2000
	s_nop 0
	global_load_lds_dwordx4 v150, s[46:47]
	s_add_u32 s46, s42, 0x40000
	s_addc_u32 s47, s43, 0
	s_add_i32 s64, s59, s48
	s_mov_b32 m0, s64
	s_nop 0
	global_load_lds_dwordx4 v148, s[46:47]
	s_add_i32 m0, s64, 0x2000
	s_nop 0
	global_load_lds_dwordx4 v150, s[46:47]
	s_add_u32 s46, s6, s25
	s_addc_u32 s47, s7, s27
	s_mov_b64 s[64:65], s[46:47]
	s_mov_b32 m0, s1
	s_nop 0
	global_load_lds_dwordx4 v132, s[64:65]
	s_mov_b32 m0, s11
	s_nop 0
	global_load_lds_dwordx4 v133, s[64:65]
	s_cmp_lg_u64 s[14:15], 0
	s_cbranch_scc0 .Lgw_p7_1
	s_waitcnt vmcnt(8)
.Lgw_p7_1:
	s_waitcnt lgkmcnt(0)
	s_barrier
	s_setprio 1
	s_waitcnt lgkmcnt(0)
	v_mfma_scale_f32_16x16x128_f8f6f4 v[64:67], v[136:143], v[68:75], v[64:67], v153, v153 op_sel_hi:[0,0,0]
	v_mfma_scale_f32_16x16x128_f8f6f4 v[60:63], v[160:167], v[68:75], v[60:63], v153, v153 op_sel_hi:[0,0,0]
	v_mfma_scale_f32_16x16x128_f8f6f4 v[56:59], v[136:143], v[76:83], v[56:59], v153, v153 op_sel_hi:[0,0,0]
	v_mfma_scale_f32_16x16x128_f8f6f4 v[52:55], v[160:167], v[76:83], v[52:55], v153, v153 op_sel_hi:[0,0,0]
	v_mfma_scale_f32_16x16x128_f8f6f4 v[212:215], v[136:143], v[84:91], v[48:51], v153, v153 op_sel_hi:[0,0,0]
	v_mfma_scale_f32_16x16x128_f8f6f4 v[216:219], v[160:167], v[84:91], v[44:47], v153, v153 op_sel_hi:[0,0,0]
	v_mfma_scale_f32_16x16x128_f8f6f4 v[220:223], v[136:143], v[92:99], v[40:43], v153, v153 op_sel_hi:[0,0,0]
	v_mfma_scale_f32_16x16x128_f8f6f4 v[224:227], v[160:167], v[92:99], v[36:39], v153, v153 op_sel_hi:[0,0,0]
	s_setprio 0
	s_setprio 1
	v_mfma_scale_f32_16x16x128_f8f6f4 v[232:235], v[176:183], v[68:75], v[232:235], v153, v153 op_sel_hi:[0,0,0]
	v_mfma_scale_f32_16x16x128_f8f6f4 v[228:231], v[168:175], v[68:75], v[32:35], v153, v153 op_sel_hi:[0,0,0]
	v_mfma_scale_f32_16x16x128_f8f6f4 v[236:239], v[168:175], v[76:83], v[24:27], v153, v153 op_sel_hi:[0,0,0]
	v_mfma_scale_f32_16x16x128_f8f6f4 v[240:243], v[176:183], v[76:83], v[20:23], v153, v153 op_sel_hi:[0,0,0]
	v_mfma_scale_f32_16x16x128_f8f6f4 v[244:247], v[168:175], v[84:91], v[16:19], v153, v153 op_sel_hi:[0,0,0]
	v_mfma_scale_f32_16x16x128_f8f6f4 v[248:251], v[176:183], v[84:91], v[12:15], v153, v153 op_sel_hi:[0,0,0]
	v_mfma_scale_f32_16x16x128_f8f6f4 v[154:157], v[168:175], v[92:99], v[8:11], v153, v153 op_sel_hi:[0,0,0]
	v_mfma_scale_f32_16x16x128_f8f6f4 v[68:71], v[176:183], v[92:99], v[4:7], v153, v153 op_sel_hi:[0,0,0]
	s_setprio 0
	s_waitcnt vmcnt(8)
	s_barrier
	s_add_i32 s25, 0, 0x18000
	v_add_u32_e32 v1, s25, v158
	s_add_i32 s27, 0, 0x1c000
	s_nop 1
	ds_read_b128 v[4:7], v1
	ds_read_b128 v[8:11], v1 offset:1024
	ds_read_b128 v[12:15], v1 offset:2048
	ds_read_b128 v[16:19], v1 offset:3072
	v_add_u32_e32 v1, s27, v158
	ds_read_b128 v[136:139], v1
	ds_read_b128 v[140:143], v1 offset:1024
	ds_read_b128 v[160:163], v1 offset:2048
	ds_read_b128 v[164:167], v1 offset:3072
	s_mov_b64 s[64:65], s[46:47]
	s_mov_b32 m0, s50
	ds_read_b128 v[20:23], v151 offset:32768
	ds_read_b128 v[24:27], v151 offset:33792
	ds_read_b128 v[28:31], v151 offset:34816
	ds_read_b128 v[32:35], v151 offset:35840
	ds_read_b128 v[36:39], v151 offset:36864
	ds_read_b128 v[40:43], v151 offset:37888
	ds_read_b128 v[44:47], v151 offset:38912
	ds_read_b128 v[48:51], v151 offset:39936
	s_nop 0
	global_load_lds_dwordx4 v134, s[64:65]
	s_mov_b32 m0, s51
	s_nop 0
	global_load_lds_dwordx4 v135, s[64:65]
	s_cmp_lg_u64 s[14:15], 0
	s_cbranch_scc0 .Lgw_p7_2
	s_waitcnt vmcnt(8)
.Lgw_p7_2:
	s_waitcnt lgkmcnt(0)
	s_barrier
	s_setprio 1
	s_waitcnt lgkmcnt(0)
	v_mfma_scale_f32_16x16x128_f8f6f4 v[128:131], v[4:11], v[20:27], v[128:131], v153, v153 op_sel_hi:[0,0,0]
	v_mfma_scale_f32_16x16x128_f8f6f4 v[124:127], v[12:19], v[20:27], v[124:127], v153, v153 op_sel_hi:[0,0,0]
	v_mfma_scale_f32_16x16x128_f8f6f4 v[120:123], v[4:11], v[28:35], v[120:123], v153, v153 op_sel_hi:[0,0,0]
	v_mfma_scale_f32_16x16x128_f8f6f4 v[116:119], v[12:19], v[28:35], v[116:119], v153, v153 op_sel_hi:[0,0,0]
	v_mfma_scale_f32_16x16x128_f8f6f4 v[112:115], v[4:11], v[36:43], v[112:115], v153, v153 op_sel_hi:[0,0,0]
	v_mfma_scale_f32_16x16x128_f8f6f4 v[108:111], v[12:19], v[36:43], v[108:111], v153, v153 op_sel_hi:[0,0,0]
	v_mfma_scale_f32_16x16x128_f8f6f4 v[104:107], v[4:11], v[44:51], v[104:107], v153, v153 op_sel_hi:[0,0,0]
	v_mfma_scale_f32_16x16x128_f8f6f4 v[100:103], v[12:19], v[44:51], v[100:103], v153, v153 op_sel_hi:[0,0,0]
	s_setprio 0
	s_setprio 1
	v_mfma_scale_f32_16x16x128_f8f6f4 v[96:99], v[136:143], v[20:27], v[144:147], v153, v153 op_sel_hi:[0,0,0]
	v_mfma_scale_f32_16x16x128_f8f6f4 v[92:95], v[160:167], v[20:27], v[184:187], v153, v153 op_sel_hi:[0,0,0]
	v_mfma_scale_f32_16x16x128_f8f6f4 v[88:91], v[136:143], v[28:35], v[188:191], v153, v153 op_sel_hi:[0,0,0]
	v_mfma_scale_f32_16x16x128_f8f6f4 v[84:87], v[160:167], v[28:35], v[192:195], v153, v153 op_sel_hi:[0,0,0]
	v_mfma_scale_f32_16x16x128_f8f6f4 v[80:83], v[136:143], v[36:43], v[196:199], v153, v153 op_sel_hi:[0,0,0]
	v_mfma_scale_f32_16x16x128_f8f6f4 v[76:79], v[160:167], v[36:43], v[200:203], v153, v153 op_sel_hi:[0,0,0]
	v_mfma_scale_f32_16x16x128_f8f6f4 v[72:75], v[136:143], v[44:51], v[204:207], v153, v153 op_sel_hi:[0,0,0]
	v_mfma_scale_f32_16x16x128_f8f6f4 v[28:31], v[160:167], v[44:51], v[208:211], v153, v153 op_sel_hi:[0,0,0]
	s_setprio 0
	s_waitcnt vmcnt(8)
	s_barrier
	s_add_i32 s25, s25, s48
	s_mov_b32 m0, s25
	ds_read_b128 v[20:23], v151 offset:49152
	ds_read_b128 v[24:27], v151 offset:50176
	ds_read_b128 v[168:171], v151 offset:51200
	ds_read_b128 v[172:175], v151 offset:52224
	ds_read_b128 v[176:179], v151 offset:53248
	ds_read_b128 v[180:183], v151 offset:54272
	ds_read_b128 v[184:187], v151 offset:55296
	ds_read_b128 v[188:191], v151 offset:56320
	s_nop 0
	global_load_lds_dwordx4 v148, s[44:45]
	s_add_i32 m0, s25, 0x2000
	s_add_u32 s42, s42, 0x40080
	s_addc_u32 s43, s43, 0
	s_add_i32 s25, s27, s48
	global_load_lds_dwordx4 v150, s[44:45]
	s_mov_b32 m0, s25
	s_nop 0
	global_load_lds_dwordx4 v148, s[42:43]
	s_add_i32 m0, s25, 0x2000
	s_nop 0
	global_load_lds_dwordx4 v150, s[42:43]
	s_add_u32 s42, s46, 0x80
	s_addc_u32 s43, s47, 0
	s_mov_b32 m0, s56
	s_nop 0
	global_load_lds_dwordx4 v132, s[42:43]
	s_mov_b32 m0, s57
	s_nop 0
	global_load_lds_dwordx4 v133, s[42:43]
	s_cmp_lg_u64 s[14:15], 0
	s_cbranch_scc0 .Lgw_p7_3
	s_waitcnt vmcnt(8)
.Lgw_p7_3:
	s_waitcnt lgkmcnt(0)
	s_barrier
	s_setprio 1
	s_waitcnt lgkmcnt(0)
	v_mfma_scale_f32_16x16x128_f8f6f4 v[64:67], v[4:11], v[20:27], v[64:67], v153, v153 op_sel_hi:[0,0,0]
	v_mfma_scale_f32_16x16x128_f8f6f4 v[60:63], v[12:19], v[20:27], v[60:63], v153, v153 op_sel_hi:[0,0,0]
	v_mfma_scale_f32_16x16x128_f8f6f4 v[56:59], v[4:11], v[168:175], v[56:59], v153, v153 op_sel_hi:[0,0,0]
	v_mfma_scale_f32_16x16x128_f8f6f4 v[52:55], v[12:19], v[168:175], v[52:55], v153, v153 op_sel_hi:[0,0,0]
	v_mfma_scale_f32_16x16x128_f8f6f4 v[48:51], v[4:11], v[176:183], v[212:215], v153, v153 op_sel_hi:[0,0,0]
	v_mfma_scale_f32_16x16x128_f8f6f4 v[44:47], v[12:19], v[176:183], v[216:219], v153, v153 op_sel_hi:[0,0,0]
	v_mfma_scale_f32_16x16x128_f8f6f4 v[40:43], v[4:11], v[184:191], v[220:223], v153, v153 op_sel_hi:[0,0,0]
	v_mfma_scale_f32_16x16x128_f8f6f4 v[36:39], v[12:19], v[184:191], v[224:227], v153, v153 op_sel_hi:[0,0,0]
	s_setprio 0
	s_setprio 1
	v_mfma_scale_f32_16x16x128_f8f6f4 v[32:35], v[136:143], v[20:27], v[228:231], v153, v153 op_sel_hi:[0,0,0]
	v_mfma_scale_f32_16x16x128_f8f6f4 v[232:235], v[160:167], v[20:27], v[232:235], v153, v153 op_sel_hi:[0,0,0]
	v_mfma_scale_f32_16x16x128_f8f6f4 v[24:27], v[136:143], v[168:175], v[236:239], v153, v153 op_sel_hi:[0,0,0]
	v_mfma_scale_f32_16x16x128_f8f6f4 v[20:23], v[160:167], v[168:175], v[240:243], v153, v153 op_sel_hi:[0,0,0]
	v_mfma_scale_f32_16x16x128_f8f6f4 v[16:19], v[136:143], v[176:183], v[244:247], v153, v153 op_sel_hi:[0,0,0]
	v_mfma_scale_f32_16x16x128_f8f6f4 v[12:15], v[160:167], v[176:183], v[248:251], v153, v153 op_sel_hi:[0,0,0]
	v_mfma_scale_f32_16x16x128_f8f6f4 v[8:11], v[136:143], v[184:191], v[154:157], v153, v153 op_sel_hi:[0,0,0]
	v_mfma_scale_f32_16x16x128_f8f6f4 v[4:7], v[160:167], v[184:191], v[68:71], v153, v153 op_sel_hi:[0,0,0]
	s_setprio 0
	s_waitcnt vmcnt(8)
	s_barrier
	s_add_i32 s23, s23, 2
	s_add_u32 s40, s40, 0x100
	s_addc_u32 s41, s41, 0
	s_cmp_gt_u32 s23, 13
	s_cbranch_scc1 .LBB0_1048
